# speedup vs baseline: 1.0300x; 1.0300x over previous
.LBB4_18:
.LBB4_24:
	s_and_b64 s[50:51], s[42:43], exec
	s_cselect_b32 s52, s39, s47
	s_cselect_b32 s53, s38, s46
	s_cselect_b32 s54, s41, s45
	s_cselect_b32 s55, s40, s44
	s_add_u32 s28, s46, 0x100
	s_addc_u32 s84, s47, 0
	s_and_b64 s[50:51], s[48:49], exec
	s_cselect_b32 s51, s52, s84
	s_cselect_b32 s50, s53, s28
	s_add_u32 s28, s44, 0x100
	s_addc_u32 s84, s45, 0
	s_and_b64 s[48:49], s[48:49], exec
	s_cselect_b32 s49, s54, s84
	s_cselect_b32 s48, s55, s28
	s_mov_b32 m0, s59
	v_add_u32_e32 v229, s76, v234
	v_lshl_add_u64 v[130:131], s[48:49], 0, v[216:217]
	ds_read_b128 v[74:77], v229
	ds_read_b128 v[86:89], v229 offset:1024
	ds_read_b128 v[98:101], v229 offset:2048
	ds_read_b128 v[106:109], v229 offset:3072
	global_load_lds_dwordx4 v[130:131], off
	v_lshl_add_u64 v[132:133], s[48:49], 0, v[218:219]
	s_mov_b32 m0, s60
	s_nop 0
	global_load_lds_dwordx4 v[132:133], off
	s_barrier
	s_waitcnt lgkmcnt(0)
	s_setprio 1
	s_waitcnt lgkmcnt(0)
	v_mfma_f32_16x16x32_f16 v[94:97], v[74:77], v[46:49], 0
	v_mfma_f32_16x16x32_f16 v[46:49], v[98:101], v[46:49], 0
	v_mfma_f32_16x16x32_f16 v[94:97], v[86:89], v[50:53], v[94:97]
	v_mfma_f32_16x16x32_f16 v[50:53], v[106:109], v[50:53], v[46:49]
	v_mfma_f32_16x16x32_f16 v[46:49], v[74:77], v[38:41], 0
	v_mfma_f32_16x16x32_f16 v[38:41], v[98:101], v[38:41], 0
	v_mfma_f32_16x16x32_f16 v[110:113], v[106:109], v[42:45], v[38:41]
	v_mfma_f32_16x16x32_f16 v[38:41], v[74:77], v[30:33], 0
	v_mfma_f32_16x16x32_f16 v[30:33], v[98:101], v[30:33], 0
	v_mfma_f32_16x16x32_f16 v[174:177], v[106:109], v[34:37], v[30:33]
	v_mfma_f32_16x16x32_f16 v[30:33], v[74:77], v[22:25], 0
	v_mfma_f32_16x16x32_f16 v[22:25], v[98:101], v[22:25], 0
	v_mfma_f32_16x16x32_f16 v[102:105], v[86:89], v[42:45], v[46:49]
	v_mfma_f32_16x16x32_f16 v[170:173], v[86:89], v[34:37], v[38:41]
	v_mfma_f32_16x16x32_f16 v[178:181], v[86:89], v[26:29], v[30:33]
	v_mfma_f32_16x16x32_f16 v[182:185], v[106:109], v[26:29], v[22:25]
	s_setprio 0
	s_mov_b32 m0, s58
	s_barrier
	ds_read_b128 v[34:37], v237 offset:16384
	ds_read_b128 v[46:49], v237 offset:17408
	ds_read_b128 v[114:117], v237 offset:18432
	ds_read_b128 v[118:121], v237 offset:19456
	ds_read_b128 v[122:125], v237 offset:20480
	ds_read_b128 v[126:129], v237 offset:21504
	ds_read_b128 v[166:169], v237 offset:22528
	ds_read_b128 v[186:189], v237 offset:23552
	global_load_lds_dwordx4 v220, s[50:51]
	s_mov_b32 m0, s62
	s_nop 0
	global_load_lds_dwordx4 v226, s[50:51]
	s_barrier
	s_waitcnt lgkmcnt(0)
	s_setprio 1
	s_waitcnt lgkmcnt(0)
	v_mfma_f32_16x16x32_f16 v[22:25], v[6:9], v[34:37], 0
	v_mfma_f32_16x16x32_f16 v[30:33], v[6:9], v[114:117], 0
	v_mfma_f32_16x16x32_f16 v[42:45], v[6:9], v[122:125], 0
	v_mfma_f32_16x16x32_f16 v[6:9], v[6:9], v[166:169], 0
	v_mfma_f32_16x16x32_f16 v[22:25], v[10:13], v[46:49], v[22:25]
	v_mfma_f32_16x16x32_f16 v[26:29], v[14:17], v[34:37], 0
	v_mfma_f32_16x16x32_f16 v[30:33], v[10:13], v[118:121], v[30:33]
	v_mfma_f32_16x16x32_f16 v[38:41], v[14:17], v[114:117], 0
	v_mfma_f32_16x16x32_f16 v[42:45], v[10:13], v[126:129], v[42:45]
	v_mfma_f32_16x16x32_f16 v[134:137], v[14:17], v[122:125], 0
	v_mfma_f32_16x16x32_f16 v[6:9], v[10:13], v[186:189], v[6:9]
	v_mfma_f32_16x16x32_f16 v[10:13], v[14:17], v[166:169], 0
	v_mfma_f32_16x16x32_f16 v[26:29], v[18:21], v[46:49], v[26:29]
	v_mfma_f32_16x16x32_f16 v[38:41], v[18:21], v[118:121], v[38:41]
	v_mfma_f32_16x16x32_f16 v[134:137], v[18:21], v[126:129], v[134:137]
	v_mfma_f32_16x16x32_f16 v[14:17], v[18:21], v[186:189], v[10:13]
	s_setprio 0
	s_barrier
	s_add_u32 s86, s48, 0x40000
	s_addc_u32 s87, s49, 0
	s_add_i32 s84, s76, s57
	v_lshl_add_u64 v[10:11], s[86:87], 0, v[216:217]
	s_mov_b32 m0, s84
	s_add_i32 s85, s84, 0x2000
	global_load_lds_dwordx4 v[10:11], off
	v_lshl_add_u64 v[10:11], s[86:87], 0, v[218:219]
	s_mov_b32 m0, s85
	s_nop 0
	global_load_lds_dwordx4 v[10:11], off
	s_add_i32 s94, s61, s33
	s_mov_b32 s95, 0
	s_cmpk_gt_u32 s94, 0x15ff
	s_cselect_b64 s[96:97], -1, 0
	s_and_b64 s[96:97], s[96:97], exec
	s_cselect_b32 s96, 0x7fffea00, 0
	s_cselect_b32 s98, s25, s15
	s_cselect_b32 s99, s24, s14
	s_add_i32 s96, s96, s94
	s_lshl_b32 s94, s96, 1
	s_addk_i32 s94, 0x2c00
	s_lshl_b64 s[96:97], s[94:95], 12
	s_add_u32 s100, s99, s96
	s_addc_u32 s101, s98, s97
	s_add_i32 s94, s75, s61
	s_cmpk_gt_u32 s94, 0x15ff
	s_cselect_b32 s97, 0x7fffea00, 0
	s_cselect_b32 s96, 0x80, 0
	s_add_i32 s97, s97, s94
	s_lshl_b32 s94, s97, 1
	s_add_i32 s97, s94, 0x2c00
	s_mul_hi_u32 s98, s97, 0xba2e8ba3
	s_lshr_b32 s98, s98, 11
	s_mul_i32 s99, s98, 0x7ffff500
	s_add_i32 s99, s99, s97
	s_lshr_b32 s97, s99, 7
	s_mul_i32 s98, s98, 22
	s_add_i32 s97, s97, s98
	s_lshl_b32 s97, s97, 8
	s_and_b32 s94, s94, 0x7e
	s_or_b32 s96, s97, s96
	s_or_b32 s94, s96, s94
	s_lshl_b64 s[96:97], s[94:95], 11
	s_add_i32 s94, s61, -1
	s_cmp_lt_u32 s94, 43
	s_waitcnt vmcnt(6)
	s_cbranch_scc0 .Lhka_rare_a0
	v_cvt_pk_f16_f32 v2, v2, v3
	v_cvt_pk_f16_f32 v3, v4, v5
	v_lshl_add_u64 v[4:5], v[224:225], 0, s[96:97]
	global_store_dwordx2 v[4:5], v[2:3], off
	v_lshlrev_b32_e32 v4, 2, v214
	global_load_dwordx4 v[2:5], v4, s[100:101] nt
	s_add_i32 s61, s61, 1

.LBB4_30:
	v_mov_b32_e32 v227, v221
	v_lshl_add_u64 v[54:55], s[50:51], 0, v[220:221]
	v_lshl_add_u64 v[56:57], s[50:51], 0, v[226:227]
	s_add_i32 s50, 0, 0x1c000
	s_mov_b32 m0, s67
	v_add_u32_e32 v238, s50, v234
	v_lshl_add_u64 v[58:59], v[130:131], 0, s[30:31]
	ds_read_b128 v[240:243], v238
	ds_read_b128 v[244:247], v238 offset:1024
	ds_read_b128 v[248:251], v238 offset:2048
	ds_read_b128 v[252:255], v238 offset:3072
	global_load_lds_dwordx4 v[58:59], off
	v_lshl_add_u64 v[58:59], v[132:133], 0, s[30:31]
	s_mov_b32 m0, s68
	s_nop 0
	global_load_lds_dwordx4 v[58:59], off
	s_barrier
	s_waitcnt lgkmcnt(0)
	s_setprio 1
	s_waitcnt lgkmcnt(0)
	v_mfma_f32_16x16x32_f16 v[58:61], v[240:243], v[122:125], v[94:97]
	v_mfma_f32_16x16x32_f16 v[50:53], v[248:251], v[122:125], v[50:53]
	v_mfma_f32_16x16x32_f16 v[130:133], v[244:247], v[126:129], v[58:61]
	v_mfma_f32_16x16x32_f16 v[126:129], v[252:255], v[126:129], v[50:53]
	v_mfma_f32_16x16x32_f16 v[50:53], v[240:243], v[118:121], v[102:105]
	v_mfma_f32_16x16x32_f16 v[122:125], v[244:247], v[210:213], v[50:53]
	v_mfma_f32_16x16x32_f16 v[50:53], v[248:251], v[118:121], v[110:113]
	v_mfma_f32_16x16x32_f16 v[118:121], v[252:255], v[210:213], v[50:53]
	v_mfma_f32_16x16x32_f16 v[50:53], v[240:243], v[202:205], v[170:173]
	v_mfma_f32_16x16x32_f16 v[110:113], v[244:247], v[206:209], v[50:53]
	v_mfma_f32_16x16x32_f16 v[50:53], v[248:251], v[202:205], v[174:177]
	v_mfma_f32_16x16x32_f16 v[102:105], v[252:255], v[206:209], v[50:53]
	v_mfma_f32_16x16x32_f16 v[50:53], v[240:243], v[18:21], v[178:181]
	v_mfma_f32_16x16x32_f16 v[18:21], v[248:251], v[18:21], v[182:185]
	v_mfma_f32_16x16x32_f16 v[94:97], v[244:247], v[198:201], v[50:53]
	v_mfma_f32_16x16x32_f16 v[82:85], v[252:255], v[198:201], v[18:21]
	s_setprio 0
	s_mov_b32 m0, s69
	s_nop 3
	v_lshl_add_u64 v[18:19], v[54:55], 0, s[30:31]
	s_barrier
	ds_read_b128 v[66:69], v237 offset:49152
	ds_read_b128 v[78:81], v237 offset:50176
	ds_read_b128 v[170:173], v237 offset:51200
	ds_read_b128 v[174:177], v237 offset:52224
	ds_read_b128 v[178:181], v237 offset:53248
	ds_read_b128 v[182:185], v237 offset:54272
	ds_read_b128 v[198:201], v237 offset:55296
	ds_read_b128 v[202:205], v237 offset:56320
	global_load_lds_dwordx4 v[18:19], off
	v_lshl_add_u64 v[18:19], v[56:57], 0, s[30:31]
	s_mov_b32 m0, s70
	s_nop 0
	global_load_lds_dwordx4 v[18:19], off
	s_barrier
	s_waitcnt lgkmcnt(0)
	s_setprio 1
	s_waitcnt lgkmcnt(0)
	v_mfma_f32_16x16x32_f16 v[18:21], v[10:13], v[66:69], v[22:25]
	v_mfma_f32_16x16x32_f16 v[70:73], v[186:189], v[78:81], v[18:21]
	v_mfma_f32_16x16x32_f16 v[18:21], v[190:193], v[66:69], v[26:29]
	v_mfma_f32_16x16x32_f16 v[58:61], v[194:197], v[78:81], v[18:21]
	v_mfma_f32_16x16x32_f16 v[18:21], v[10:13], v[170:173], v[30:33]
	v_mfma_f32_16x16x32_f16 v[50:53], v[186:189], v[174:177], v[18:21]
	v_mfma_f32_16x16x32_f16 v[18:21], v[190:193], v[170:173], v[38:41]
	v_mfma_f32_16x16x32_f16 v[38:41], v[194:197], v[174:177], v[18:21]
	v_mfma_f32_16x16x32_f16 v[18:21], v[10:13], v[178:181], v[42:45]
	v_mfma_f32_16x16x32_f16 v[6:9], v[10:13], v[198:201], v[6:9]
	v_mfma_f32_16x16x32_f16 v[26:29], v[186:189], v[182:185], v[18:21]
	v_mfma_f32_16x16x32_f16 v[18:21], v[190:193], v[178:181], v[134:137]
	v_mfma_f32_16x16x32_f16 v[10:13], v[186:189], v[202:205], v[6:9]
	v_mfma_f32_16x16x32_f16 v[6:9], v[190:193], v[198:201], v[14:17]
	v_mfma_f32_16x16x32_f16 v[18:21], v[194:197], v[182:185], v[18:21]
	v_mfma_f32_16x16x32_f16 v[6:9], v[194:197], v[202:205], v[6:9]
	s_setprio 0
	s_barrier
	s_add_u32 s48, s48, 0x40080
	s_addc_u32 s49, s49, 0
	s_add_i32 s50, s50, s57
	v_lshl_add_u64 v[14:15], s[48:49], 0, v[216:217]
	s_mov_b32 m0, s50
	s_add_i32 s51, s50, 0x2000
	global_load_lds_dwordx4 v[14:15], off
	v_lshl_add_u64 v[14:15], s[48:49], 0, v[218:219]
	s_mov_b32 m0, s51
	s_nop 0
	global_load_lds_dwordx4 v[14:15], off
	s_add_i32 s94, s61, s33
	s_mov_b32 s95, 0
	s_cmpk_gt_u32 s94, 0x15ff
	s_cselect_b64 s[96:97], -1, 0
	s_and_b64 s[96:97], s[96:97], exec
	s_cselect_b32 s96, 0x7fffea00, 0
	s_cselect_b32 s98, s25, s15
	s_cselect_b32 s99, s24, s14
	s_add_i32 s96, s96, s94
	s_lshl_b32 s94, s96, 1
	s_addk_i32 s94, 0x2c00
	s_lshl_b64 s[96:97], s[94:95], 12
	s_add_u32 s100, s99, s96
	s_addc_u32 s101, s98, s97
	s_add_i32 s94, s75, s61
	s_cmpk_gt_u32 s94, 0x15ff
	s_cselect_b32 s97, 0x7fffea00, 0
	s_cselect_b32 s96, 0x80, 0
	s_add_i32 s97, s97, s94
	s_lshl_b32 s94, s97, 1
	s_add_i32 s97, s94, 0x2c00
	s_mul_hi_u32 s98, s97, 0xba2e8ba3
	s_lshr_b32 s98, s98, 11
	s_mul_i32 s99, s98, 0x7ffff500
	s_add_i32 s99, s99, s97
	s_lshr_b32 s97, s99, 7
	s_mul_i32 s98, s98, 22
	s_add_i32 s97, s97, s98
	s_lshl_b32 s97, s97, 8
	s_and_b32 s94, s94, 0x7e
	s_or_b32 s96, s97, s96
	s_or_b32 s94, s96, s94
	s_lshl_b64 s[96:97], s[94:95], 11
	s_add_i32 s94, s61, -1
	s_cmp_lt_u32 s94, 43
	s_waitcnt vmcnt(6)
	s_cbranch_scc0 .Lhka_rare_a1
	v_cvt_pk_f16_f32 v2, v2, v3
	v_cvt_pk_f16_f32 v3, v4, v5
	v_lshl_add_u64 v[4:5], v[224:225], 0, s[96:97]
	global_store_dwordx2 v[4:5], v[2:3], off
	v_lshlrev_b32_e32 v4, 2, v214
	global_load_dwordx4 v[2:5], v4, s[100:101] nt
	s_add_i32 s61, s61, 1

.LBB4_40:
	s_add_u32 s28, s46, 0x80
	s_addc_u32 s48, s47, 0
	s_and_b64 s[44:45], s[44:45], exec
	s_cselect_b32 s45, s54, s87
	s_cselect_b32 s44, s55, s86
	s_mov_b32 m0, s59
	v_lshl_add_u64 v[182:183], s[44:45], 0, v[216:217]
	ds_read_b128 v[186:189], v229
	ds_read_b128 v[190:193], v229 offset:1024
	ds_read_b128 v[194:197], v229 offset:2048
	ds_read_b128 v[198:201], v229 offset:3072
	global_load_lds_dwordx4 v[182:183], off
	v_lshl_add_u64 v[184:185], s[44:45], 0, v[218:219]
	s_mov_b32 m0, s60
	s_cselect_b32 s49, s52, s48
	global_load_lds_dwordx4 v[184:185], off
	s_barrier
	s_waitcnt lgkmcnt(0)
	s_cselect_b32 s48, s53, s28
	s_setprio 1
	s_waitcnt lgkmcnt(0)
	v_mfma_f32_16x16x32_f16 v[130:133], v[186:189], v[174:177], v[130:133]
	v_mfma_f32_16x16x32_f16 v[126:129], v[194:197], v[174:177], v[126:129]
	v_mfma_f32_16x16x32_f16 v[122:125], v[186:189], v[166:169], v[122:125]
	v_mfma_f32_16x16x32_f16 v[118:121], v[194:197], v[166:169], v[118:121]
	v_mfma_f32_16x16x32_f16 v[110:113], v[186:189], v[158:161], v[110:113]
	v_mfma_f32_16x16x32_f16 v[102:105], v[194:197], v[158:161], v[102:105]
	v_mfma_f32_16x16x32_f16 v[94:97], v[186:189], v[150:153], v[94:97]
	v_mfma_f32_16x16x32_f16 v[82:85], v[194:197], v[150:153], v[82:85]
	v_mfma_f32_16x16x32_f16 v[130:133], v[190:193], v[178:181], v[130:133]
	v_mfma_f32_16x16x32_f16 v[126:129], v[198:201], v[178:181], v[126:129]
	v_mfma_f32_16x16x32_f16 v[122:125], v[190:193], v[170:173], v[122:125]
	v_mfma_f32_16x16x32_f16 v[118:121], v[198:201], v[170:173], v[118:121]
	v_mfma_f32_16x16x32_f16 v[110:113], v[190:193], v[162:165], v[110:113]
	v_mfma_f32_16x16x32_f16 v[102:105], v[198:201], v[162:165], v[102:105]
	v_mfma_f32_16x16x32_f16 v[94:97], v[190:193], v[154:157], v[94:97]
	v_mfma_f32_16x16x32_f16 v[82:85], v[198:201], v[154:157], v[82:85]
	s_setprio 0
	s_mov_b32 m0, s58
	s_barrier
	ds_read_b128 v[150:153], v237 offset:16384
	ds_read_b128 v[154:157], v237 offset:17408
	ds_read_b128 v[158:161], v237 offset:18432
	ds_read_b128 v[162:165], v237 offset:19456
	ds_read_b128 v[166:169], v237 offset:20480
	ds_read_b128 v[170:173], v237 offset:21504
	ds_read_b128 v[174:177], v237 offset:22528
	ds_read_b128 v[178:181], v237 offset:23552
	global_load_lds_dwordx4 v220, s[48:49]
	s_mov_b32 m0, s62
	s_nop 0
	global_load_lds_dwordx4 v226, s[48:49]
	s_barrier
	s_waitcnt lgkmcnt(0)
	s_setprio 1
	s_waitcnt lgkmcnt(0)
	v_mfma_f32_16x16x32_f16 v[70:73], v[134:137], v[150:153], v[70:73]
	v_mfma_f32_16x16x32_f16 v[58:61], v[142:145], v[150:153], v[58:61]
	v_mfma_f32_16x16x32_f16 v[50:53], v[134:137], v[158:161], v[50:53]
	v_mfma_f32_16x16x32_f16 v[38:41], v[142:145], v[158:161], v[38:41]
	v_mfma_f32_16x16x32_f16 v[26:29], v[134:137], v[166:169], v[26:29]
	v_mfma_f32_16x16x32_f16 v[18:21], v[142:145], v[166:169], v[18:21]
	v_mfma_f32_16x16x32_f16 v[10:13], v[134:137], v[174:177], v[10:13]
	v_mfma_f32_16x16x32_f16 v[6:9], v[142:145], v[174:177], v[6:9]
	v_mfma_f32_16x16x32_f16 v[70:73], v[138:141], v[154:157], v[70:73]
	v_mfma_f32_16x16x32_f16 v[58:61], v[146:149], v[154:157], v[58:61]
	v_mfma_f32_16x16x32_f16 v[50:53], v[138:141], v[162:165], v[50:53]
	v_mfma_f32_16x16x32_f16 v[38:41], v[146:149], v[162:165], v[38:41]
	v_mfma_f32_16x16x32_f16 v[26:29], v[138:141], v[170:173], v[26:29]
	v_mfma_f32_16x16x32_f16 v[18:21], v[146:149], v[170:173], v[18:21]
	v_mfma_f32_16x16x32_f16 v[10:13], v[138:141], v[178:181], v[10:13]
	v_mfma_f32_16x16x32_f16 v[6:9], v[146:149], v[178:181], v[6:9]
	s_setprio 0
	s_barrier
	s_add_u32 s90, s44, 0x40000
	s_addc_u32 s91, s45, 0
	s_mov_b32 m0, s84
	v_lshl_add_u64 v[134:135], s[90:91], 0, v[216:217]
	global_load_lds_dwordx4 v[134:135], off
	v_lshl_add_u64 v[134:135], s[90:91], 0, v[218:219]
	s_mov_b32 m0, s85
	s_nop 0
	global_load_lds_dwordx4 v[134:135], off
	s_add_i32 s94, s61, s33
	s_mov_b32 s95, 0
	s_cmpk_gt_u32 s94, 0x15ff
	s_cselect_b64 s[96:97], -1, 0
	s_and_b64 s[96:97], s[96:97], exec
	s_cselect_b32 s96, 0x7fffea00, 0
	s_cselect_b32 s98, s25, s15
	s_cselect_b32 s99, s24, s14
	s_add_i32 s96, s96, s94
	s_lshl_b32 s94, s96, 1
	s_addk_i32 s94, 0x2c00
	s_lshl_b64 s[96:97], s[94:95], 12
	s_add_u32 s100, s99, s96
	s_addc_u32 s101, s98, s97
	s_add_i32 s94, s75, s61
	s_cmpk_gt_u32 s94, 0x15ff
	s_cselect_b32 s97, 0x7fffea00, 0
	s_cselect_b32 s96, 0x80, 0
	s_add_i32 s97, s97, s94
	s_lshl_b32 s94, s97, 1
	s_add_i32 s97, s94, 0x2c00
	s_mul_hi_u32 s98, s97, 0xba2e8ba3
	s_lshr_b32 s98, s98, 11
	s_mul_i32 s99, s98, 0x7ffff500
	s_add_i32 s99, s99, s97
	s_lshr_b32 s97, s99, 7
	s_mul_i32 s98, s98, 22
	s_add_i32 s97, s97, s98
	s_lshl_b32 s97, s97, 8
	s_and_b32 s94, s94, 0x7e
	s_or_b32 s96, s97, s96
	s_or_b32 s94, s96, s94
	s_lshl_b64 s[96:97], s[94:95], 11
	s_add_i32 s94, s61, -1
	s_cmp_lt_u32 s94, 43
	s_waitcnt vmcnt(6)
	s_cbranch_scc0 .Lhka_rare_a2
	v_cvt_pk_f16_f32 v2, v2, v3
	v_cvt_pk_f16_f32 v3, v4, v5
	v_lshl_add_u64 v[4:5], v[224:225], 0, s[96:97]
	global_store_dwordx2 v[4:5], v[2:3], off
	v_lshlrev_b32_e32 v4, 2, v214
	global_load_dwordx4 v[2:5], v4, s[100:101] nt
	s_add_i32 s61, s61, 1

.LBB4_46:
	s_mov_b32 m0, s67
	v_lshl_add_u64 v[182:183], v[182:183], 0, s[30:31]
	ds_read_b128 v[190:193], v238
	ds_read_b128 v[194:197], v238 offset:1024
	ds_read_b128 v[198:201], v238 offset:2048
	ds_read_b128 v[202:205], v238 offset:3072
	global_load_lds_dwordx4 v[182:183], off
	v_lshl_add_u64 v[182:183], v[184:185], 0, s[30:31]
	s_mov_b32 m0, s68
	v_mov_b32_e32 v227, v221
	global_load_lds_dwordx4 v[182:183], off
	s_barrier
	s_waitcnt lgkmcnt(0)
	v_lshl_add_u64 v[186:187], s[48:49], 0, v[220:221]
	v_lshl_add_u64 v[188:189], s[48:49], 0, v[226:227]
	s_setprio 1
	s_waitcnt lgkmcnt(0)
	v_mfma_f32_16x16x32_f16 v[130:133], v[190:193], v[174:177], v[130:133]
	v_mfma_f32_16x16x32_f16 v[126:129], v[198:201], v[174:177], v[126:129]
	v_mfma_f32_16x16x32_f16 v[122:125], v[190:193], v[166:169], v[122:125]
	v_mfma_f32_16x16x32_f16 v[118:121], v[198:201], v[166:169], v[118:121]
	v_mfma_f32_16x16x32_f16 v[110:113], v[190:193], v[158:161], v[110:113]
	v_mfma_f32_16x16x32_f16 v[102:105], v[198:201], v[158:161], v[102:105]
	v_mfma_f32_16x16x32_f16 v[94:97], v[190:193], v[150:153], v[94:97]
	v_mfma_f32_16x16x32_f16 v[82:85], v[198:201], v[150:153], v[82:85]
	v_mfma_f32_16x16x32_f16 v[130:133], v[194:197], v[178:181], v[130:133]
	v_mfma_f32_16x16x32_f16 v[126:129], v[202:205], v[178:181], v[126:129]
	v_mfma_f32_16x16x32_f16 v[122:125], v[194:197], v[170:173], v[122:125]
	v_mfma_f32_16x16x32_f16 v[118:121], v[202:205], v[170:173], v[118:121]
	v_mfma_f32_16x16x32_f16 v[110:113], v[194:197], v[162:165], v[110:113]
	v_mfma_f32_16x16x32_f16 v[102:105], v[202:205], v[162:165], v[102:105]
	v_mfma_f32_16x16x32_f16 v[94:97], v[194:197], v[154:157], v[94:97]
	v_mfma_f32_16x16x32_f16 v[82:85], v[202:205], v[154:157], v[82:85]
	s_setprio 0
	s_mov_b32 m0, s69
	v_lshl_add_u64 v[182:183], v[186:187], 0, s[30:31]
	s_barrier
	ds_read_b128 v[150:153], v237 offset:49152
	ds_read_b128 v[154:157], v237 offset:50176
	ds_read_b128 v[158:161], v237 offset:51200
	ds_read_b128 v[162:165], v237 offset:52224
	ds_read_b128 v[166:169], v237 offset:53248
	ds_read_b128 v[170:173], v237 offset:54272
	ds_read_b128 v[174:177], v237 offset:55296
	ds_read_b128 v[178:181], v237 offset:56320
	global_load_lds_dwordx4 v[182:183], off
	v_lshl_add_u64 v[182:183], v[188:189], 0, s[30:31]
	s_mov_b32 m0, s70
	s_nop 0
	global_load_lds_dwordx4 v[182:183], off
	s_barrier
	s_waitcnt lgkmcnt(0)
	s_setprio 1
	s_waitcnt lgkmcnt(0)
	v_mfma_f32_16x16x32_f16 v[70:73], v[134:137], v[150:153], v[70:73]
	v_mfma_f32_16x16x32_f16 v[58:61], v[142:145], v[150:153], v[58:61]
	v_mfma_f32_16x16x32_f16 v[50:53], v[134:137], v[158:161], v[50:53]
	v_mfma_f32_16x16x32_f16 v[38:41], v[142:145], v[158:161], v[38:41]
	v_mfma_f32_16x16x32_f16 v[26:29], v[134:137], v[166:169], v[26:29]
	v_mfma_f32_16x16x32_f16 v[18:21], v[142:145], v[166:169], v[18:21]
	v_mfma_f32_16x16x32_f16 v[10:13], v[134:137], v[174:177], v[10:13]
	v_mfma_f32_16x16x32_f16 v[6:9], v[142:145], v[174:177], v[6:9]
	v_mfma_f32_16x16x32_f16 v[70:73], v[138:141], v[154:157], v[70:73]
	v_mfma_f32_16x16x32_f16 v[58:61], v[146:149], v[154:157], v[58:61]
	v_mfma_f32_16x16x32_f16 v[50:53], v[138:141], v[162:165], v[50:53]
	v_mfma_f32_16x16x32_f16 v[38:41], v[146:149], v[162:165], v[38:41]
	v_mfma_f32_16x16x32_f16 v[26:29], v[138:141], v[170:173], v[26:29]
	v_mfma_f32_16x16x32_f16 v[18:21], v[146:149], v[170:173], v[18:21]
	v_mfma_f32_16x16x32_f16 v[10:13], v[138:141], v[178:181], v[10:13]
	v_mfma_f32_16x16x32_f16 v[6:9], v[146:149], v[178:181], v[6:9]
	s_setprio 0
	s_barrier
	s_add_u32 s44, s44, 0x40080
	s_addc_u32 s45, s45, 0
	s_mov_b32 m0, s50
	v_lshl_add_u64 v[134:135], s[44:45], 0, v[216:217]
	global_load_lds_dwordx4 v[134:135], off
	v_lshl_add_u64 v[134:135], s[44:45], 0, v[218:219]
	s_mov_b32 m0, s51
	s_nop 0
	global_load_lds_dwordx4 v[134:135], off
	s_add_i32 s94, s61, s33
	s_mov_b32 s95, 0
	s_cmpk_gt_u32 s94, 0x15ff
	s_cselect_b64 s[96:97], -1, 0
	s_and_b64 s[96:97], s[96:97], exec
	s_cselect_b32 s96, 0x7fffea00, 0
	s_cselect_b32 s98, s25, s15
	s_cselect_b32 s99, s24, s14
	s_add_i32 s96, s96, s94
	s_lshl_b32 s94, s96, 1
	s_addk_i32 s94, 0x2c00
	s_lshl_b64 s[96:97], s[94:95], 12
	s_add_u32 s100, s99, s96
	s_addc_u32 s101, s98, s97
	s_add_i32 s94, s75, s61
	s_cmpk_gt_u32 s94, 0x15ff
	s_cselect_b32 s97, 0x7fffea00, 0
	s_cselect_b32 s96, 0x80, 0
	s_add_i32 s97, s97, s94
	s_lshl_b32 s94, s97, 1
	s_add_i32 s97, s94, 0x2c00
	s_mul_hi_u32 s98, s97, 0xba2e8ba3
	s_lshr_b32 s98, s98, 11
	s_mul_i32 s99, s98, 0x7ffff500
	s_add_i32 s99, s99, s97
	s_lshr_b32 s97, s99, 7
	s_mul_i32 s98, s98, 22
	s_add_i32 s97, s97, s98
	s_lshl_b32 s97, s97, 8
	s_and_b32 s94, s94, 0x7e
	s_or_b32 s96, s97, s96
	s_or_b32 s94, s96, s94
	s_lshl_b64 s[96:97], s[94:95], 11
	s_add_i32 s28, s88, 2
	s_add_u32 s46, s46, 0x100
	s_addc_u32 s47, s47, 0
	s_add_u32 s86, s86, 0x100
	s_addc_u32 s87, s87, 0
	s_add_i32 s94, s61, -1
	s_cmp_lt_u32 s94, 43
	s_waitcnt vmcnt(6)
	s_cbranch_scc0 .Lhka_rare_a3
	v_cvt_pk_f16_f32 v2, v2, v3
	v_cvt_pk_f16_f32 v3, v4, v5
	v_lshl_add_u64 v[4:5], v[224:225], 0, s[96:97]
	global_store_dwordx2 v[4:5], v[2:3], off
	v_lshlrev_b32_e32 v4, 2, v214
	global_load_dwordx4 v[2:5], v4, s[100:101] nt
	s_add_i32 s61, s61, 1

.Lhka_rld_a0:
	s_cmp_eq_u32 s61, 44
	s_cbranch_scc1 .Lhka_rinc_a0
	v_lshlrev_b32_e32 v4, 2, v214
	global_load_dwordx4 v[2:5], v4, s[100:101] nt
